# C1 + grid barriers: the acquire invalidate (buffer_inv sc1) is issued just before the arrive atomic, after the workgroup's own loads have drained; its latency hides under the arrive round trip and the
# baseline (speedup 1.0000x reference)
.LBB0_61:
	s_mov_b64 s[8:9], exec
	v_readlane_b32 s2, v255, 6
	s_lshl_b32 s3, s2, 8
	v_readlane_b32 s6, v255, 4
	v_mbcnt_lo_u32_b32 v2, s8, 0
	v_readlane_b32 s7, v255, 5
	s_add_u32 s6, s6, s3
	v_mbcnt_hi_u32_b32 v2, s9, v2
	s_addc_u32 s7, s7, 0
	v_cmp_eq_u32_e32 vcc, 0, v2
	s_and_saveexec_b64 s[10:11], vcc
	s_cbranch_execz .LBB0_63
	s_bcnt1_i32_b64 s3, s[8:9]
	v_mov_b32_e32 v4, 0x1000
	v_mov_b32_e32 v5, s3
	buffer_inv sc1
	global_atomic_add v4, v4, v5, s[6:7] offset:1024 sc0

.LBB0_156:
	s_mov_b64 s[10:11], exec
	v_readlane_b32 s2, v255, 6
	s_lshl_b32 s3, s2, 8
	v_readlane_b32 s8, v255, 4
	v_mbcnt_lo_u32_b32 v2, s10, 0
	v_readlane_b32 s9, v255, 5
	s_add_u32 s8, s8, s3
	v_mbcnt_hi_u32_b32 v2, s11, v2
	s_addc_u32 s9, s9, 0
	v_cmp_eq_u32_e32 vcc, 0, v2
	s_and_saveexec_b64 s[12:13], vcc
	s_cbranch_execz .LBB0_158
	s_bcnt1_i32_b64 s3, s[10:11]
	v_mov_b32_e32 v4, 0x1000
	v_mov_b32_e32 v5, s3
	buffer_inv sc1
	global_atomic_add v4, v4, v5, s[8:9] offset:1024 sc0

.LBB0_610:
	s_mov_b64 s[8:9], exec
	v_readlane_b32 s2, v255, 6
	s_lshl_b32 s2, s2, 8
	v_readlane_b32 s6, v255, 4
	v_mbcnt_lo_u32_b32 v2, s8, 0
	v_readlane_b32 s7, v255, 5
	s_add_u32 s6, s6, s2
	v_mbcnt_hi_u32_b32 v2, s9, v2
	s_addc_u32 s7, s7, 0
	v_cmp_eq_u32_e32 vcc, 0, v2
	s_and_saveexec_b64 s[10:11], vcc
	s_cbranch_execz .LBB0_612
	s_bcnt1_i32_b64 s2, s[8:9]
	v_mov_b32_e32 v4, 0x1000
	v_mov_b32_e32 v5, s2
	buffer_inv sc1
	global_atomic_add v4, v4, v5, s[6:7] offset:1024 sc0

.LBB0_1162:
	s_mov_b64 s[8:9], exec
	v_readlane_b32 s2, v255, 6
	s_lshl_b32 s2, s2, 8
	v_readlane_b32 s4, v255, 4
	v_mbcnt_lo_u32_b32 v2, s8, 0
	v_readlane_b32 s5, v255, 5
	s_add_u32 s4, s4, s2
	v_mbcnt_hi_u32_b32 v2, s9, v2
	s_addc_u32 s5, s5, 0
	v_cmp_eq_u32_e32 vcc, 0, v2
	s_and_saveexec_b64 s[10:11], vcc
	s_cbranch_execz .LBB0_1164
	s_bcnt1_i32_b64 s2, s[8:9]
	v_mov_b32_e32 v4, 0x1000
	v_mov_b32_e32 v5, s2
	buffer_inv sc1
	global_atomic_add v4, v4, v5, s[4:5] offset:1024 sc0

.LBB0_1261:
	s_mov_b64 s[10:11], exec
	v_readlane_b32 s2, v255, 6
	s_lshl_b32 s2, s2, 8
	v_readlane_b32 s8, v255, 4
	v_mbcnt_lo_u32_b32 v2, s10, 0
	v_readlane_b32 s9, v255, 5
	s_add_u32 s8, s8, s2
	v_mbcnt_hi_u32_b32 v2, s11, v2
	s_addc_u32 s9, s9, 0
	v_cmp_eq_u32_e32 vcc, 0, v2
	s_and_saveexec_b64 s[12:13], vcc
	s_cbranch_execz .LBB0_1263
	s_bcnt1_i32_b64 s2, s[10:11]
	v_mov_b32_e32 v4, 0x1000
	v_mov_b32_e32 v5, s2
	buffer_inv sc1
	global_atomic_add v4, v4, v5, s[8:9] offset:1024 sc0

.LBB0_1430:
	s_mov_b64 s[18:19], exec
	v_readlane_b32 s2, v255, 6
	s_lshl_b32 s2, s2, 8
	v_readlane_b32 s10, v255, 4
	v_mbcnt_lo_u32_b32 v2, s18, 0
	v_readlane_b32 s11, v255, 5
	s_add_u32 s10, s10, s2
	v_mbcnt_hi_u32_b32 v2, s19, v2
	s_addc_u32 s11, s11, 0
	v_cmp_eq_u32_e32 vcc, 0, v2
	s_and_saveexec_b64 s[30:31], vcc
	s_cbranch_execz .LBB0_1432
	s_bcnt1_i32_b64 s2, s[18:19]
	v_mov_b32_e32 v4, 0x1000
	v_mov_b32_e32 v5, s2
	buffer_inv sc1
	global_atomic_add v4, v4, v5, s[10:11] offset:1024 sc0

.LBB0_1680:
	s_mov_b64 s[6:7], exec
	v_readlane_b32 s4, v255, 6
	s_lshl_b32 s4, s4, 8
	v_readlane_b32 s8, v255, 4
	v_mbcnt_lo_u32_b32 v1, s6, 0
	v_readlane_b32 s9, v255, 5
	s_add_u32 s4, s8, s4
	v_mbcnt_hi_u32_b32 v1, s7, v1
	s_addc_u32 s5, s9, 0
	v_cmp_eq_u32_e32 vcc, 0, v1
	s_and_saveexec_b64 s[8:9], vcc
	s_cbranch_execz .LBB0_1682
	s_bcnt1_i32_b64 s6, s[6:7]
	v_mov_b32_e32 v3, 0x1000
	v_mov_b32_e32 v4, s6
	buffer_inv sc1
	global_atomic_add v3, v3, v4, s[4:5] offset:1024 sc0
